# grid barrier: L1 invalidate (acquire) issued at arrival by wave 1 instead of by the leader after the flip
# speedup vs baseline: 1.0130x; 1.0002x over previous
.LBB0_139:
	s_waitcnt vmcnt(0)
	s_barrier
	s_cmp_lg_u32 s80, 64
	s_cbranch_scc1 .Lxb_acq_0
	buffer_inv sc1
	s_waitcnt vmcnt(0)
.Lxb_acq_0:
	s_and_saveexec_b64 s[0:1], s[4:5]
	s_cbranch_execz .LBB0_189
	s_add_i32 s3, 0, 0x20000
	v_mov_b32_e32 v0, s3
	s_waitcnt vmcnt(0) expcnt(0) lgkmcnt(0)
	ds_read_b32 v2, v0
	s_add_i32 s3, 0, 0x20004
	v_mov_b32_e32 v0, s3
	ds_read_b32 v0, v0
	s_waitcnt lgkmcnt(1)
	v_cmp_ne_u32_e32 vcc, 0, v2
	s_cbranch_vccnz .LBB0_155
	v_readlane_b32 s4, v249, 0
	v_readlane_b32 s5, v249, 1
	s_load_dwordx2 s[8:9], s[4:5], 0x4
	s_add_u32 s4, s56, 0x1000
	s_addc_u32 s5, s57, 0
	s_add_u32 s6, s56, 0x1100
	s_addc_u32 s7, s57, 0
	s_waitcnt lgkmcnt(0)
	s_mul_i32 s3, s8, s34
	s_add_u32 s8, s56, 0x1200
	s_mul_i32 s3, s3, s9
	s_addc_u32 s9, s57, 0
	s_add_u32 s10, s56, 0x1300
	s_addc_u32 s11, s57, 0
	s_mov_b32 s33, 1
	v_mov_b32_e32 v16, 0
	s_branch .LBB0_143

.LBB0_170:
	s_or_b64 exec, exec, s[6:7]
	s_waitcnt vmcnt(0)
	s_waitcnt vmcnt(0)

.LBB0_188:
	s_or_b64 exec, exec, s[4:5]
	s_waitcnt vmcnt(0)
	s_waitcnt vmcnt(0)

.LBB0_266:
	s_waitcnt vmcnt(0)
	s_waitcnt vmcnt(16) lgkmcnt(0)
	s_barrier
	v_readlane_b32 s98, v249, 3
	s_nop 0
	s_cmp_lg_u32 s98, 1
	s_cbranch_scc1 .Lxb_acq_1
	buffer_inv sc1
	s_waitcnt vmcnt(0)

.LBB0_416:
	s_waitcnt vmcnt(0)
	s_barrier
	v_readlane_b32 s98, v249, 3
	s_nop 0
	s_cmp_lg_u32 s98, 1
	s_cbranch_scc1 .Lxb_acq_2
	buffer_inv sc1
	s_waitcnt vmcnt(0)
.Lxb_acq_2:
	s_and_saveexec_b64 s[0:1], s[4:5]
	s_cbranch_execz .LBB0_466
	s_add_i32 s3, 0, 0x20000
	s_waitcnt vmcnt(6)
	v_mov_b32_e32 v0, s3
	s_waitcnt vmcnt(0) expcnt(0) lgkmcnt(0)
	ds_read_b32 v2, v0
	s_add_i32 s3, 0, 0x20004
	v_mov_b32_e32 v0, s3
	ds_read_b32 v0, v0
	s_waitcnt lgkmcnt(1)
	v_cmp_ne_u32_e32 vcc, 0, v2
	s_cbranch_vccnz .LBB0_432
	v_readlane_b32 s4, v249, 0
	v_readlane_b32 s5, v249, 1
	s_load_dwordx2 s[8:9], s[4:5], 0x4
	s_add_u32 s4, s56, 0x1000
	s_addc_u32 s5, s57, 0
	s_add_u32 s6, s56, 0x1100
	s_addc_u32 s7, s57, 0
	s_waitcnt lgkmcnt(0)
	s_mul_i32 s3, s8, s34
	s_add_u32 s8, s56, 0x1200
	s_mul_i32 s3, s3, s9
	s_addc_u32 s9, s57, 0
	s_add_u32 s10, s56, 0x1300
	s_addc_u32 s11, s57, 0
	s_mov_b32 s33, 1
	v_mov_b32_e32 v16, 0
	s_branch .LBB0_420

.Lxb_acq_3:
	s_and_saveexec_b64 s[0:1], s[4:5]
	s_cbranch_execz .LBB0_562
	s_add_i32 s3, 0, 0x20000
	s_waitcnt vmcnt(4)
	v_mov_b32_e32 v0, s3
	s_waitcnt vmcnt(0) expcnt(0) lgkmcnt(0)
	ds_read_b32 v2, v0
	s_add_i32 s3, 0, 0x20004
	v_mov_b32_e32 v0, s3
	ds_read_b32 v0, v0
	s_waitcnt lgkmcnt(1)
	v_cmp_ne_u32_e32 vcc, 0, v2
	s_cbranch_vccnz .LBB0_528
	v_readlane_b32 s4, v249, 0
	v_readlane_b32 s5, v249, 1
	s_load_dwordx2 s[8:9], s[4:5], 0x4
	s_add_u32 s4, s56, 0x1000
	s_addc_u32 s5, s57, 0
	s_add_u32 s6, s56, 0x1100
	s_addc_u32 s7, s57, 0
	s_waitcnt lgkmcnt(0)
	s_mul_i32 s3, s8, s34
	s_add_u32 s8, s56, 0x1200
	s_mul_i32 s3, s3, s9
	s_addc_u32 s9, s57, 0
	s_add_u32 s10, s56, 0x1300
	s_addc_u32 s11, s57, 0
	s_mov_b32 s33, 1
	v_mov_b32_e32 v16, 0
	s_branch .LBB0_516

.LBB0_669:
	s_waitcnt vmcnt(0)
	s_waitcnt lgkmcnt(0)
	s_barrier
	v_readlane_b32 s98, v249, 3
	s_nop 0
	s_cmp_lg_u32 s98, 1
	s_cbranch_scc1 .Lxb_acq_4
	buffer_inv sc1
	s_waitcnt vmcnt(0)

.Lxb_acq_5:
	s_and_saveexec_b64 s[0:1], s[8:9]
	s_cbranch_execz .LBB0_814
	s_add_i32 s8, 0, 0x20000
	v_mov_b32_e32 v0, s8
	s_waitcnt vmcnt(0) expcnt(0) lgkmcnt(0)
	ds_read_b32 v2, v0
	s_add_i32 s8, 0, 0x20004
	v_mov_b32_e32 v0, s8
	ds_read_b32 v0, v0
	s_waitcnt lgkmcnt(1)
	v_cmp_ne_u32_e32 vcc, 0, v2
	s_cbranch_vccnz .LBB0_780
	v_readlane_b32 s8, v249, 0
	v_readlane_b32 s9, v249, 1
	s_load_dwordx2 s[12:13], s[8:9], 0x4
	s_add_u32 s8, s56, 0x1000
	s_addc_u32 s9, s57, 0
	s_add_u32 s10, s56, 0x1100
	s_addc_u32 s11, s57, 0
	s_waitcnt lgkmcnt(0)
	s_mul_i32 s33, s12, s34
	s_add_u32 s12, s56, 0x1200
	s_mul_i32 s33, s33, s13
	s_addc_u32 s13, s57, 0
	s_add_u32 s14, s56, 0x1300
	s_addc_u32 s15, s57, 0
	s_mov_b32 s40, 1
	v_mov_b32_e32 v16, 0
	s_branch .LBB0_768

.LBB0_795:
	s_or_b64 exec, exec, s[10:11]
	s_waitcnt vmcnt(0)
	s_waitcnt vmcnt(0)

.LBB0_813:
	s_or_b64 exec, exec, s[8:9]
	s_waitcnt vmcnt(0)
	s_waitcnt vmcnt(0)

.Lxb_acq_7:
	s_and_saveexec_b64 s[0:1], s[4:5]
	s_cbranch_execz .LBB0_1045
	s_add_i32 s3, 0, 0x20000
	s_waitcnt vmcnt(6)
	v_mov_b32_e32 v0, s3
	s_waitcnt vmcnt(0) expcnt(0) lgkmcnt(0)
	ds_read_b32 v2, v0
	s_add_i32 s3, 0, 0x20004
	v_mov_b32_e32 v0, s3
	ds_read_b32 v0, v0
	s_waitcnt lgkmcnt(1)
	v_cmp_ne_u32_e32 vcc, 0, v2
	s_cbranch_vccnz .LBB0_1011
	v_readlane_b32 s4, v249, 0
	v_readlane_b32 s5, v249, 1
	s_load_dwordx2 s[8:9], s[4:5], 0x4
	s_add_u32 s4, s56, 0x1000
	s_addc_u32 s5, s57, 0
	s_add_u32 s6, s56, 0x1100
	s_addc_u32 s7, s57, 0
	s_waitcnt lgkmcnt(0)
	s_mul_i32 s3, s8, s34
	s_add_u32 s8, s56, 0x1200
	s_mul_i32 s3, s3, s9
	s_addc_u32 s9, s57, 0
	s_add_u32 s10, s56, 0x1300
	s_addc_u32 s11, s57, 0
	s_mov_b32 s20, 1
	v_mov_b32_e32 v16, 0
	s_branch .LBB0_999

.Lxb_acq_8:
	s_and_saveexec_b64 s[0:1], s[4:5]
	s_cbranch_execz .LBB0_1171
	s_add_i32 s3, 0, 0x20000
	v_mov_b32_e32 v0, s3
	s_waitcnt vmcnt(0) expcnt(0) lgkmcnt(0)
	ds_read_b32 v2, v0
	s_add_i32 s3, 0, 0x20004
	v_mov_b32_e32 v0, s3
	ds_read_b32 v0, v0
	s_waitcnt lgkmcnt(1)
	v_cmp_ne_u32_e32 vcc, 0, v2
	s_cbranch_vccnz .LBB0_1137
	v_readlane_b32 s4, v249, 0
	v_readlane_b32 s5, v249, 1
	s_load_dwordx2 s[8:9], s[4:5], 0x4
	s_add_u32 s4, s56, 0x1000
	s_addc_u32 s5, s57, 0
	s_add_u32 s6, s56, 0x1100
	s_addc_u32 s7, s57, 0
	s_waitcnt lgkmcnt(0)
	s_mul_i32 s3, s8, s34
	s_add_u32 s8, s56, 0x1200
	s_mul_i32 s3, s3, s9
	s_addc_u32 s9, s57, 0
	s_add_u32 s10, s56, 0x1300
	s_addc_u32 s11, s57, 0
	s_mov_b32 s18, 1
	v_mov_b32_e32 v16, 0
	s_branch .LBB0_1125

.LBB0_1380:
	s_waitcnt vmcnt(0)
	s_waitcnt vmcnt(8) lgkmcnt(0)
	s_barrier
	v_readlane_b32 s98, v249, 3
	s_nop 0
	s_cmp_lg_u32 s98, 1
	s_cbranch_scc1 .Lxb_acq_10
	buffer_inv sc1
	s_waitcnt vmcnt(0)
.Lxb_acq_10:
	s_and_saveexec_b64 s[0:1], s[10:11]
	s_cbranch_execz .LBB0_1430
	s_add_i32 s10, 0, 0x20000
	v_mov_b32_e32 v0, s10
	s_waitcnt vmcnt(0) expcnt(0) lgkmcnt(0)
	ds_read_b32 v2, v0
	s_add_i32 s10, 0, 0x20004
	v_mov_b32_e32 v0, s10
	ds_read_b32 v0, v0
	s_waitcnt lgkmcnt(1)
	v_cmp_ne_u32_e32 vcc, 0, v2
	s_cbranch_vccnz .LBB0_1396
	v_readlane_b32 s10, v249, 0
	v_readlane_b32 s11, v249, 1
	s_load_dwordx2 s[24:25], s[10:11], 0x4
	s_add_u32 s10, s56, 0x1000
	s_addc_u32 s11, s57, 0
	s_add_u32 s12, s56, 0x1100
	s_addc_u32 s13, s57, 0
	s_waitcnt lgkmcnt(0)
	s_mul_i32 s33, s24, s34
	s_add_u32 s24, s56, 0x1200
	s_mul_i32 s33, s33, s25
	s_addc_u32 s25, s57, 0
	s_add_u32 s26, s56, 0x1300
	s_addc_u32 s27, s57, 0
	s_mov_b32 s40, 1
	v_mov_b32_e32 v16, 0
	s_branch .LBB0_1384

.LBB0_1411:
	s_or_b64 exec, exec, s[12:13]
	s_waitcnt vmcnt(0)
	s_waitcnt vmcnt(0)

	.amdhsa_kernel _Z6mk_fwd6Params
		.amdhsa_group_segment_fixed_size 0
		.amdhsa_private_segment_fixed_size 0
		.amdhsa_kernarg_size 416
		.amdhsa_user_sgpr_count 2
		.amdhsa_user_sgpr_dispatch_ptr 0
		.amdhsa_user_sgpr_queue_ptr 0
		.amdhsa_user_sgpr_kernarg_segment_ptr 1
		.amdhsa_user_sgpr_dispatch_id 0
		.amdhsa_user_sgpr_kernarg_preload_length 0
		.amdhsa_user_sgpr_kernarg_preload_offset 0
		.amdhsa_user_sgpr_private_segment_size 0
		.amdhsa_uses_dynamic_stack 0
		.amdhsa_enable_private_segment 0
		.amdhsa_system_sgpr_workgroup_id_x 1
		.amdhsa_system_sgpr_workgroup_id_y 0
		.amdhsa_system_sgpr_workgroup_id_z 0
		.amdhsa_system_sgpr_workgroup_info 0
		.amdhsa_system_vgpr_workitem_id 0
		.amdhsa_next_free_vgpr 252
		.amdhsa_next_free_sgpr 99
		.amdhsa_accum_offset 252
		.amdhsa_reserve_vcc 1
		.amdhsa_float_round_mode_32 0
		.amdhsa_float_round_mode_16_64 0
		.amdhsa_float_denorm_mode_32 3
		.amdhsa_float_denorm_mode_16_64 3
		.amdhsa_dx10_clamp 1
		.amdhsa_ieee_mode 1
		.amdhsa_fp16_overflow 0
		.amdhsa_tg_split 0
		.amdhsa_exception_fp_ieee_invalid_op 0
		.amdhsa_exception_fp_denorm_src 0
		.amdhsa_exception_fp_ieee_div_zero 0
		.amdhsa_exception_fp_ieee_overflow 0
		.amdhsa_exception_fp_ieee_underflow 0
		.amdhsa_exception_fp_ieee_inexact 0
		.amdhsa_exception_int_div_zero 0
	.end_amdhsa_kernel

amdhsa.kernels:
  - .agpr_count:     0
    .args:
      - .offset:         0
        .size:           160
        .value_kind:     by_value
      - .offset:         160
        .size:           4
        .value_kind:     hidden_block_count_x
      - .offset:         164
        .size:           4
        .value_kind:     hidden_block_count_y
      - .offset:         168
        .size:           4
        .value_kind:     hidden_block_count_z
      - .offset:         172
        .size:           2
        .value_kind:     hidden_group_size_x
      - .offset:         174
        .size:           2
        .value_kind:     hidden_group_size_y
      - .offset:         176
        .size:           2
        .value_kind:     hidden_group_size_z
      - .offset:         178
        .size:           2
        .value_kind:     hidden_remainder_x
      - .offset:         180
        .size:           2
        .value_kind:     hidden_remainder_y
      - .offset:         182
        .size:           2
        .value_kind:     hidden_remainder_z
      - .offset:         200
        .size:           8
        .value_kind:     hidden_global_offset_x
      - .offset:         208
        .size:           8
        .value_kind:     hidden_global_offset_y
      - .offset:         216
        .size:           8
        .value_kind:     hidden_global_offset_z
      - .offset:         224
        .size:           2
        .value_kind:     hidden_grid_dims
      - .offset:         280
        .size:           4
        .value_kind:     hidden_dynamic_lds_size
    .group_segment_fixed_size: 0
    .kernarg_segment_align: 8
    .kernarg_segment_size: 416
    .language:       OpenCL C
    .language_version:
      - 2
      - 0
    .max_flat_workgroup_size: 512
    .name:           _Z6mk_fwd6Params
    .private_segment_fixed_size: 0
    .sgpr_count:     105
    .sgpr_spill_count: 14
    .symbol:         _Z6mk_fwd6Params.kd
    .uniform_work_group_size: 1
    .uses_dynamic_stack: false
    .vgpr_count:     252
    .vgpr_spill_count: 0
    .wavefront_size: 64
